# gate/up expert GEMM: the four gathered-row index loads per unit issued together (one wait instead of four round trips)
# speedup vs baseline: 1.0064x; 1.0064x over previous
; template <class Sched, class Epi, bool FP8 = false>
; DEVI void gemm_phase(LAS unsigned char* lds, const int K, const Sched& S, const Epi& E) {
;     ...
;         const bool has_next = S.next(ui + 1, nxt);
;         if (has_next) S.aoff(nxt, R0, C0, R1, C1, vn);
;     DEVI unsigned one(const pg8::Unit& u, int R, int C) const { const int slot = u.pm * 256 + R; const int row = (slot < mvalid) ? selrow[u.e * MSLOT + slot] : 0; return (unsigned)(row * (DM / 2) + C) * 2u; }
;     DEVI void aoff(const pg8::Unit& u, int R0, int C0, int R1, int C1, unsigned (&o)[4]) const { o[0] = one(u, R0, C0); o[1] = one(u, R1, C1); o[2] = one(u, 128 + R0, C0); o[3] = one(u, 128 + R1, C1); }
.LBB0_1257:
	v_cndmask_b32_e64 v1, 0, 1, s[28:29]
	v_cmp_ne_u32_e64 s[38:39], 1, v1
	s_andn2_b64 vcc, exec, s[28:29]
	v_mov_b32_e32 v251, v206
	v_mov_b32_e32 v252, v204
	v_mov_b32_e32 v1, v202
	v_mov_b32_e32 v228, v208
	s_mov_b64 s[62:63], s[66:67]
	s_mov_b64 s[64:65], s[16:17]
	s_cbranch_vccnz .LBB0_1267
	s_lshl_b32 s4, s6, 8
	s_mul_i32 s5, s58, 0x500
	v_readlane_b32 s34, v254, 24
	v_readlane_b32 s35, v254, 25
	v_add_u32_e32 v10, s4, v197
	v_add_u32_e32 v12, s4, v220
	v_add_u32_e32 v14, s4, v221
	v_add_u32_e32 v16, s4, v241
	v_mov_b32_e32 v4, 0
	v_mov_b32_e32 v5, 0
	v_mov_b32_e32 v1, 0
	v_mov_b32_e32 v6, 0
	v_cmp_gt_i32_e32 vcc, s47, v10
	v_add_u32_e32 v10, s5, v10
	v_ashrrev_i32_e32 v11, 31, v10
	v_lshl_add_u64 v[10:11], v[10:11], 2, s[34:35]
	s_and_saveexec_b64 s[28:29], vcc
	global_load_dword v4, v[10:11], off
	s_or_b64 exec, exec, s[28:29]
	v_cmp_gt_i32_e32 vcc, s47, v12
	v_add_u32_e32 v12, s5, v12
	v_ashrrev_i32_e32 v13, 31, v12
	v_lshl_add_u64 v[12:13], v[12:13], 2, s[34:35]
	s_and_saveexec_b64 s[28:29], vcc
	global_load_dword v5, v[12:13], off
	s_or_b64 exec, exec, s[28:29]
	v_cmp_gt_i32_e32 vcc, s47, v14
	v_add_u32_e32 v14, s5, v14
	v_ashrrev_i32_e32 v15, 31, v14
	v_lshl_add_u64 v[14:15], v[14:15], 2, s[34:35]
	s_and_saveexec_b64 s[28:29], vcc
	global_load_dword v1, v[14:15], off
	s_or_b64 exec, exec, s[28:29]
	v_cmp_gt_i32_e32 vcc, s47, v16
	v_add_u32_e32 v16, s5, v16
	v_ashrrev_i32_e32 v17, 31, v16
	v_lshl_add_u64 v[16:17], v[16:17], 2, s[34:35]
	s_and_saveexec_b64 s[28:29], vcc
	global_load_dword v6, v[16:17], off
	s_or_b64 exec, exec, s[28:29]
	s_waitcnt vmcnt(0)
	v_lshlrev_b32_e32 v4, 10, v4
	v_lshlrev_b32_e32 v5, 10, v5
	v_lshlrev_b32_e32 v1, 10, v1
	v_lshlrev_b32_e32 v6, 10, v6
